# speedup vs baseline: 1.0545x; 1.0049x over previous
.LBB3_4:
	v_add_u32_e32 v73, s16, v72
	ds_read_b128 v[74:77], v73 offset:16384
	ds_read_b128 v[78:81], v73 offset:17408
	ds_read_b128 v[82:85], v73 offset:18432
	ds_read_b128 v[86:89], v73 offset:19456
	s_add_i32 s18, s15, 2
	s_min_i32 s18, s18, s9
	s_ashr_i32 s19, s18, 31
	s_lshl_b64 s[18:19], s[18:19], 11
	s_add_u32 s20, s4, s18
	s_addc_u32 s21, s5, s19
	s_add_i32 s17, s14, s17
	v_add_u32_e32 v118, s16, v67
	s_mov_b32 m0, s17
	ds_read_b128 v[90:93], v118
	ds_read_b128 v[94:97], v118 offset:1024
	ds_read_b128 v[98:101], v118 offset:2048
	ds_read_b128 v[102:105], v118 offset:3072
	ds_read_b128 v[106:109], v118 offset:4096
	ds_read_b128 v[110:113], v118 offset:5120
	ds_read_b128 v[114:117], v118 offset:6144
	ds_read_b128 v[118:121], v118 offset:7168
	global_load_lds_dwordx4 v68, s[20:21]
	s_add_i32 m0, s17, 0x2000
	s_add_u32 s18, s6, s18
	s_addc_u32 s19, s7, s19
	global_load_lds_dwordx4 v70, s[20:21]
	s_waitcnt vmcnt(8)
	s_barrier
	s_waitcnt lgkmcnt(0)
	s_waitcnt lgkmcnt(0)
	v_mfma_f32_16x16x32_f16 v[62:65], v[74:77], v[90:93], v[62:65]
	v_mfma_f32_16x16x32_f16 v[46:49], v[82:85], v[90:93], v[46:49]
	v_mfma_f32_16x16x32_f16 v[58:61], v[74:77], v[98:101], v[58:61]
	v_mfma_f32_16x16x32_f16 v[42:45], v[82:85], v[98:101], v[42:45]
	v_mfma_f32_16x16x32_f16 v[54:57], v[74:77], v[106:109], v[54:57]
	v_mfma_f32_16x16x32_f16 v[38:41], v[82:85], v[106:109], v[38:41]
	v_mfma_f32_16x16x32_f16 v[50:53], v[74:77], v[114:117], v[50:53]
	v_mfma_f32_16x16x32_f16 v[26:29], v[82:85], v[114:117], v[26:29]
	v_mfma_f32_16x16x32_f16 v[62:65], v[78:81], v[94:97], v[62:65]
	v_mfma_f32_16x16x32_f16 v[46:49], v[86:89], v[94:97], v[46:49]
	v_mfma_f32_16x16x32_f16 v[58:61], v[78:81], v[102:105], v[58:61]
	v_mfma_f32_16x16x32_f16 v[42:45], v[86:89], v[102:105], v[42:45]
	v_mfma_f32_16x16x32_f16 v[54:57], v[78:81], v[110:113], v[54:57]
	v_mfma_f32_16x16x32_f16 v[38:41], v[86:89], v[110:113], v[38:41]
	v_mfma_f32_16x16x32_f16 v[50:53], v[78:81], v[118:121], v[50:53]
	v_mfma_f32_16x16x32_f16 v[26:29], v[86:89], v[118:121], v[26:29]
	s_barrier
	s_add_i32 m0, s17, 0x4000
	ds_read_b128 v[74:77], v73 offset:32768
	ds_read_b128 v[78:81], v73 offset:33792
	ds_read_b128 v[82:85], v73 offset:34816
	ds_read_b128 v[86:89], v73 offset:35840
	global_load_lds_dwordx4 v68, s[18:19]
	s_add_i32 m0, s17, 0x6000
	s_nop 0
	global_load_lds_dwordx4 v70, s[18:19]
	s_add_u32 s18, s18, s2
	s_addc_u32 s19, s19, s3
	s_add_i32 m0, s17, 0x8000
	s_nop 0
	global_load_lds_dwordx4 v68, s[18:19]
	s_add_i32 m0, s17, 0xa000
	s_nop 0
	global_load_lds_dwordx4 v70, s[18:19]
	s_waitcnt vmcnt(8)
	s_barrier
	s_waitcnt lgkmcnt(0)
	s_waitcnt lgkmcnt(0)
	v_mfma_f32_16x16x32_f16 v[34:37], v[74:77], v[90:93], v[34:37]
	v_mfma_f32_16x16x32_f16 v[14:17], v[82:85], v[90:93], v[14:17]
	v_mfma_f32_16x16x32_f16 v[30:33], v[74:77], v[98:101], v[30:33]
	v_mfma_f32_16x16x32_f16 v[10:13], v[82:85], v[98:101], v[10:13]
	v_mfma_f32_16x16x32_f16 v[22:25], v[74:77], v[106:109], v[22:25]
	v_mfma_f32_16x16x32_f16 v[6:9], v[82:85], v[106:109], v[6:9]
	v_mfma_f32_16x16x32_f16 v[18:21], v[74:77], v[114:117], v[18:21]
	v_mfma_f32_16x16x32_f16 v[2:5], v[82:85], v[114:117], v[2:5]
	v_mfma_f32_16x16x32_f16 v[34:37], v[78:81], v[94:97], v[34:37]
	v_mfma_f32_16x16x32_f16 v[14:17], v[86:89], v[94:97], v[14:17]
	v_mfma_f32_16x16x32_f16 v[30:33], v[78:81], v[102:105], v[30:33]
	v_mfma_f32_16x16x32_f16 v[10:13], v[86:89], v[102:105], v[10:13]
	v_mfma_f32_16x16x32_f16 v[22:25], v[78:81], v[110:113], v[22:25]
	v_mfma_f32_16x16x32_f16 v[6:9], v[86:89], v[110:113], v[6:9]
	v_mfma_f32_16x16x32_f16 v[18:21], v[78:81], v[118:121], v[18:21]
	v_mfma_f32_16x16x32_f16 v[2:5], v[86:89], v[118:121], v[2:5]
	s_barrier
	s_add_i32 s17, s16, 0xc000
	s_cmp_lg_u32 s17, 0x24000
	s_cselect_b32 s18, s17, 0
	s_add_i32 s15, s15, 1
	s_cmp_eq_u32 s8, s15
	s_mov_b32 s17, s16
	s_mov_b32 s16, s18
	s_cbranch_scc0 .LBB3_4
	v_mov_b32_e32 v69, v5
